# speedup vs baseline: 1.0201x; 1.0201x over previous
_Z10enc_kernelPKfS0_PK15HIP_vector_typeIjLj4EES4_S4_S0_S0_S0_Pf:
	s_load_dwordx4 s[12:15], s[0:1], 0x0
	s_load_dwordx2 s[16:17], s[0:1], 0x10
	s_load_dwordx8 s[4:11], s[0:1], 0x28
	v_lshrrev_b32_e32 v56, 6, v0
	s_lshl_b32 s2, s2, 6
	v_lshl_or_b32 v47, v56, 4, s2
	v_and_b32_e32 v57, 15, v0
	v_or_b32_e32 v2, v47, v57
	v_ashrrev_i32_e32 v3, 31, v2
	s_waitcnt lgkmcnt(0)
	v_lshl_add_u64 v[4:5], v[2:3], 2, s[14:15]
	global_load_dword v46, v[4:5], off nt
	v_mov_b32_e32 v45, 0
	v_lshlrev_b64 v[2:3], 9, v[2:3]
	v_lshlrev_b32_e32 v44, 4, v0
	v_lshl_add_u64 v[2:3], s[12:13], 0, v[2:3]
	v_and_b32_e32 v48, 48, v0
	v_mov_b32_e32 v49, v45
	v_lshl_add_u64 v[42:43], v[2:3], 0, v[48:49]
	global_load_dwordx4 v[98:101], v[42:43], off nt
	global_load_dwordx4 v[102:105], v[42:43], off offset:64 nt
	global_load_dwordx4 v[106:109], v[42:43], off offset:128 nt
	global_load_dwordx4 v[110:113], v[42:43], off offset:192 nt
	global_load_dwordx4 v[10:13], v[42:43], off offset:256 nt
	global_load_dwordx4 v[14:17], v[42:43], off offset:320 nt
	s_nop 0
	global_load_dwordx4 v[2:5], v[42:43], off offset:384 nt
	global_load_dwordx4 v[6:9], v[42:43], off offset:448 nt
	v_and_b32_e32 v119, 48, v0
	global_load_dwordx4 v[120:123], v119, s[4:5]
	global_load_dwordx4 v[124:127], v119, s[4:5] offset:64
	global_load_dwordx4 v[128:131], v119, s[4:5] offset:128
	global_load_dwordx4 v[132:135], v119, s[4:5] offset:192
	global_load_dwordx4 v[136:139], v119, s[4:5] offset:256
	global_load_dwordx4 v[140:143], v119, s[4:5] offset:320
	global_load_dwordx4 v[144:147], v119, s[4:5] offset:384
	global_load_dwordx4 v[148:151], v119, s[4:5] offset:448
	global_load_dwordx4 a[0:3], v119, s[6:7]
	global_load_dwordx4 a[56:59], v119, s[6:7] offset:64
	global_load_dwordx4 a[4:7], v119, s[6:7] offset:128
	global_load_dwordx4 v[164:167], v119, s[6:7] offset:192
	global_load_dwordx4 a[32:35], v119, s[6:7] offset:256
	global_load_dwordx4 a[40:43], v119, s[6:7] offset:320
	global_load_dwordx4 a[8:11], v119, s[8:9]
	global_load_dwordx4 v[180:183], v119, s[8:9] offset:64
	global_load_dwordx4 a[12:15], v119, s[8:9] offset:128
	global_load_dwordx4 v[188:191], v119, s[8:9] offset:192
	v_lshl_add_u64 v[114:115], s[16:17], 0, v[44:45]
	s_movk_i32 s0, 0x2000
	v_add_co_u32_e32 v116, vcc, s0, v114
	s_movk_i32 s0, 0x4000
	s_nop 0
	v_addc_co_u32_e32 v117, vcc, 0, v115, vcc
	v_add_co_u32_e32 v54, vcc, s0, v114
	s_movk_i32 s0, 0x6000
	s_nop 0
	v_addc_co_u32_e32 v55, vcc, 0, v115, vcc
	global_load_dwordx4 v[18:21], v44, s[16:17]
	global_load_dwordx4 v[22:25], v[116:117], off offset:-4096
	global_load_dwordx4 v[26:29], v[116:117], off
	global_load_dwordx4 v[30:33], v[54:55], off offset:-4096
	v_add_co_u32_e32 v116, vcc, s0, v114
	s_mov_b32 s0, 0x8000
	s_nop 0
	v_addc_co_u32_e32 v117, vcc, 0, v115, vcc
	global_load_dwordx4 v[34:37], v[54:55], off
	global_load_dwordx4 v[38:41], v[116:117], off offset:-4096
	v_add_co_u32_e32 v54, vcc, s0, v114
	s_mov_b32 s0, 0xa000
	s_nop 0
	v_addc_co_u32_e32 v55, vcc, 0, v115, vcc
	global_load_dwordx4 v[50:53], v[116:117], off
	global_load_dwordx4 v[58:61], v[54:55], off offset:-4096
	v_add_co_u32_e32 v116, vcc, s0, v114
	s_mov_b32 s0, 0xc000
	s_nop 0
	v_addc_co_u32_e32 v117, vcc, 0, v115, vcc
	global_load_dwordx4 v[62:65], v[54:55], off
	global_load_dwordx4 v[66:69], v[116:117], off offset:-4096
	v_add_co_u32_e32 v54, vcc, s0, v114
	s_mov_b32 s0, 0xe000
	s_nop 0
	v_addc_co_u32_e32 v55, vcc, 0, v115, vcc
	global_load_dwordx4 v[70:73], v[116:117], off
	global_load_dwordx4 v[74:77], v[54:55], off offset:-4096
	v_add_co_u32_e32 v116, vcc, s0, v114
	s_mov_b32 s0, 0x10000
	s_nop 0
	v_addc_co_u32_e32 v117, vcc, 0, v115, vcc
	v_add_co_u32_e32 v114, vcc, s0, v114
	global_load_dwordx4 v[78:81], v[54:55], off
	global_load_dwordx4 v[82:85], v[116:117], off offset:-4096
	v_addc_co_u32_e32 v115, vcc, 0, v115, vcc
	global_load_dwordx4 v[86:89], v[116:117], off
	global_load_dwordx4 v[90:93], v[114:115], off offset:-4096
	global_load_dwordx4 v[94:97], v[114:115], off
	v_or_b32_e32 v1, 0x10000, v44
	v_and_b32_e32 v49, 63, v0
	s_movk_i32 s0, 0x1040
	s_movk_i32 s2, 0x104
	v_cmp_gt_u32_e32 vcc, 16, v49
	s_waitcnt vmcnt(16)
	ds_write_b128 v44, v[18:21]
	s_waitcnt vmcnt(15)
	ds_write_b128 v44, v[22:25] offset:4096
	s_waitcnt vmcnt(14)
	ds_write_b128 v44, v[26:29] offset:8192
	s_waitcnt vmcnt(13)
	ds_write_b128 v44, v[30:33] offset:12288
	s_waitcnt vmcnt(12)
	ds_write_b128 v44, v[34:37] offset:16384
	s_waitcnt vmcnt(11)
	ds_write_b128 v44, v[38:41] offset:20480
	s_waitcnt vmcnt(10)
	ds_write_b128 v44, v[50:53] offset:24576
	s_waitcnt vmcnt(9)
	ds_write_b128 v44, v[58:61] offset:28672
	s_waitcnt vmcnt(8)
	ds_write_b128 v44, v[62:65] offset:32768
	s_waitcnt vmcnt(7)
	ds_write_b128 v44, v[66:69] offset:36864
	s_waitcnt vmcnt(6)
	ds_write_b128 v44, v[70:73] offset:40960
	s_waitcnt vmcnt(5)
	ds_write_b128 v44, v[74:77] offset:45056
	s_waitcnt vmcnt(4)
	ds_write_b128 v44, v[78:81] offset:49152
	s_waitcnt vmcnt(3)
	ds_write_b128 v44, v[82:85] offset:53248
	s_waitcnt vmcnt(2)
	ds_write_b128 v44, v[86:89] offset:57344
	s_waitcnt vmcnt(1)
	ds_write_b128 v44, v[90:93] offset:61440
	s_waitcnt vmcnt(0)
	ds_write_b128 v1, v[94:97]
	s_waitcnt lgkmcnt(0)
	s_barrier
	s_waitcnt vmcnt(0)
	v_pk_fma_f32 v[18:19], v[98:99], -2.0, v[46:47] op_sel_hi:[1,0,0]
	v_pk_fma_f32 v[20:21], v[100:101], -2.0, v[46:47] op_sel_hi:[1,0,0]
	v_pk_fma_f32 v[22:23], v[102:103], -2.0, v[46:47] op_sel_hi:[1,0,0]
	v_pk_fma_f32 v[36:37], v[104:105], -2.0, v[46:47] op_sel_hi:[1,0,0]
	v_pk_fma_f32 v[38:39], v[106:107], -2.0, v[46:47] op_sel_hi:[1,0,0]
	v_cvt_pk_bf16_f32 v18, v18, v19
	v_cvt_pk_bf16_f32 v19, v20, v21
	v_cvt_pk_bf16_f32 v20, v22, v23
	v_cvt_pk_bf16_f32 v21, v36, v37
	v_cvt_pk_bf16_f32 v22, v38, v39
	v_lshlrev_b32_e32 v44, 4, v49
	ds_read_b128 v[58:61], v44
	ds_read_b128 v[62:65], v44 offset:1024
	ds_read_b128 v[66:69], v44 offset:4096
	ds_read_b128 v[70:73], v44 offset:5120
	ds_read_b128 v[74:77], v44 offset:8192
	ds_read_b128 v[78:81], v44 offset:9216
	ds_read_b128 v[82:85], v44 offset:12288
	ds_read_b128 v[86:89], v44 offset:13312
	v_pk_fma_f32 v[50:51], v[108:109], -2.0, v[46:47] op_sel_hi:[1,0,0]
	v_pk_fma_f32 v[52:53], v[110:111], -2.0, v[46:47] op_sel_hi:[1,0,0]
	v_pk_fma_f32 v[54:55], v[112:113], -2.0, v[46:47] op_sel_hi:[1,0,0]
	v_cvt_pk_bf16_f32 v23, v50, v51
	v_pk_fma_f32 v[0:1], v[10:11], -2.0, v[46:47] op_sel_hi:[1,0,0]
	v_pk_fma_f32 v[12:13], v[12:13], -2.0, v[46:47] op_sel_hi:[1,0,0]
	v_cvt_pk_bf16_f32 v10, v0, v1
	v_cvt_pk_bf16_f32 v11, v12, v13
	v_pk_fma_f32 v[8:9], v[8:9], -2.0, v[46:47] op_sel_hi:[1,0,0]
	v_pk_mul_f32 v[24:25], v[46:47], v[120:121] op_sel_hi:[0,1]
	v_pk_mul_f32 v[26:27], v[46:47], v[122:123] op_sel_hi:[0,1]
	v_accvgpr_write_b32 a16, v24
	v_accvgpr_write_b32 a17, v25
	v_accvgpr_write_b32 a18, v26
	v_accvgpr_write_b32 a19, v27
	v_pk_mul_f32 v[24:25], v[46:47], v[124:125] op_sel_hi:[0,1]
	v_pk_mul_f32 v[26:27], v[46:47], v[126:127] op_sel_hi:[0,1]
	v_accvgpr_write_b32 a20, v24
	v_accvgpr_write_b32 a21, v25
	v_accvgpr_write_b32 a22, v26
	v_accvgpr_write_b32 a23, v27
	v_pk_mul_f32 v[24:25], v[46:47], v[128:129] op_sel_hi:[0,1]
	v_pk_mul_f32 v[26:27], v[46:47], v[130:131] op_sel_hi:[0,1]
	v_accvgpr_write_b32 a24, v24
	v_accvgpr_write_b32 a25, v25
	v_accvgpr_write_b32 a26, v26
	v_accvgpr_write_b32 a27, v27
	v_pk_mul_f32 v[26:27], v[46:47], v[134:135] op_sel_hi:[0,1]
	v_pk_mul_f32 v[24:25], v[46:47], v[132:133] op_sel_hi:[0,1]
	v_accvgpr_write_b32 a31, v27
	v_accvgpr_write_b32 a30, v26
	v_accvgpr_write_b32 a29, v25
	v_accvgpr_write_b32 a28, v24
	v_pk_fma_f32 v[26:27], v[14:15], -2.0, v[46:47] op_sel_hi:[1,0,0]
	v_pk_fma_f32 v[28:29], v[16:17], -2.0, v[46:47] op_sel_hi:[1,0,0]
	ds_read_b128 v[14:17], v44 offset:2048
	s_waitcnt lgkmcnt(8)
	v_mfma_f32_16x16x32_bf16 a[16:19], v[58:61], v[18:21], a[16:19]
	v_cvt_pk_bf16_f32 v24, v52, v53
	v_cvt_pk_bf16_f32 v25, v54, v55
	v_cvt_pk_bf16_f32 v12, v26, v27
	s_waitcnt lgkmcnt(2)
	v_mfma_f32_16x16x32_bf16 a[28:31], v[82:85], v[18:21], a[28:31]
	v_cvt_pk_bf16_f32 v13, v28, v29
	ds_read_b128 v[26:29], v44 offset:6144
	ds_read_b128 v[40:43], v44 offset:3072
	ds_read_b128 v[50:53], v44 offset:10240
	v_mfma_f32_16x16x32_bf16 a[16:19], v[62:65], v[22:25], a[16:19]
	v_fma_f32 v34, v2, -2.0, v46
	v_fma_f32 v35, v3, -2.0, v46
	v_pk_fma_f32 v[54:55], v[6:7], -2.0, v[46:47] op_sel_hi:[1,0,0]
	v_pk_mul_f32 v[32:33], v[46:47], v[142:143] op_sel_hi:[0,1]
	s_waitcnt lgkmcnt(3)
	v_mfma_f32_16x16x32_bf16 a[16:19], v[14:17], v[10:13], a[16:19]
	ds_read_b128 v[0:3], v44 offset:7168
	ds_read_b128 v[14:17], v44 offset:14336
	v_pk_mul_f32 v[30:31], v[46:47], v[140:141] op_sel_hi:[0,1]
	v_accvgpr_write_b32 a47, v33
	v_mfma_f32_16x16x32_bf16 a[28:31], v[86:89], v[22:25], a[28:31]
	v_accvgpr_write_b32 a46, v32
	v_accvgpr_write_b32 a45, v31
	v_accvgpr_write_b32 a44, v30
	s_waitcnt lgkmcnt(0)
	v_mfma_f32_16x16x32_bf16 a[28:31], v[14:17], v[10:13], a[28:31]
	s_nop 1
	ds_read_b128 v[30:33], v44 offset:23552
	v_mfma_f32_16x16x32_bf16 a[20:23], v[66:69], v[18:21], a[20:23]
	v_mfma_f32_16x16x32_bf16 a[20:23], v[70:73], v[22:25], a[20:23]
	v_mfma_f32_16x16x32_bf16 a[20:23], v[26:29], v[10:13], a[20:23]
	v_fma_f32 v28, v4, -2.0, v46
	v_fma_f32 v29, v5, -2.0, v46
	v_cvt_pk_bf16_f32 v26, v34, v35
	v_cvt_pk_bf16_f32 v27, v28, v29
	v_cvt_pk_bf16_f32 v28, v54, v55
	v_cvt_pk_bf16_f32 v29, v8, v9
	v_mfma_f32_16x16x32_bf16 a[24:27], v[74:77], v[18:21], a[24:27]
	ds_read_b128 v[4:7], v44 offset:11264
	v_pk_mul_f32 v[34:35], v[46:47], v[136:137] op_sel_hi:[0,1]
	v_pk_mul_f32 v[36:37], v[46:47], v[138:139] op_sel_hi:[0,1]
	v_mfma_f32_16x16x32_bf16 a[20:23], v[0:3], v[26:29], a[20:23]
	s_nop 1
	v_accvgpr_write_b32 a39, v37
	v_accvgpr_write_b32 a38, v36
	v_mfma_f32_16x16x32_bf16 a[24:27], v[78:81], v[22:25], a[24:27]
	v_accvgpr_write_b32 a37, v35
	v_accvgpr_write_b32 a36, v34
	ds_read_b128 v[34:37], v44 offset:19456
	v_mfma_f32_16x16x32_bf16 a[24:27], v[50:53], v[10:13], a[24:27]
	ds_read_b128 v[50:53], v44 offset:15360
	v_pk_mul_f32 v[16:17], v[46:47], v[146:147] op_sel_hi:[0,1]
	s_waitcnt lgkmcnt(2)
	v_mfma_f32_16x16x32_bf16 a[24:27], v[4:7], v[26:29], a[24:27]
	ds_read_b128 v[4:7], v44 offset:16384
	v_pk_mul_f32 v[14:15], v[46:47], v[144:145] op_sel_hi:[0,1]
	v_accvgpr_write_b32 a51, v17
	v_mfma_f32_16x16x32_bf16 a[16:19], v[40:43], v[26:29], a[16:19]
	ds_read_b128 v[40:43], v44 offset:17408
	v_accvgpr_write_b32 a50, v16
	v_accvgpr_write_b32 a49, v15
	s_waitcnt lgkmcnt(1)
	v_mfma_f32_16x16x32_bf16 a[36:39], v[4:7], v[18:21], a[36:39]
	ds_read_b128 v[4:7], v44 offset:18432
	v_accvgpr_write_b32 a48, v14
	ds_read_b128 v[14:17], v44 offset:27648
	s_waitcnt lgkmcnt(2)
	v_mfma_f32_16x16x32_bf16 a[36:39], v[40:43], v[22:25], a[36:39]
	v_pk_mul_f32 v[2:3], v[46:47], v[150:151] op_sel_hi:[0,1]
	s_waitcnt lgkmcnt(1)
	v_mfma_f32_16x16x32_bf16 a[36:39], v[4:7], v[10:13], a[36:39]
	ds_read_b128 v[4:7], v44 offset:20480
	v_pk_mul_f32 v[0:1], v[46:47], v[148:149] op_sel_hi:[0,1]
	v_accvgpr_write_b32 a55, v3
	v_mfma_f32_16x16x32_bf16 a[36:39], v[34:37], v[26:29], a[36:39]
	ds_read_b128 v[34:37], v44 offset:21504
	v_accvgpr_write_b32 a54, v2
	v_accvgpr_write_b32 a53, v1
	s_waitcnt lgkmcnt(1)
	v_mfma_f32_16x16x32_bf16 a[44:47], v[4:7], v[18:21], a[44:47]
	ds_read_b128 v[4:7], v44 offset:22528
	v_accvgpr_write_b32 a52, v0
	ds_read_b128 v[0:3], v44 offset:30720
	s_waitcnt lgkmcnt(2)
	v_mfma_f32_16x16x32_bf16 a[44:47], v[34:37], v[22:25], a[44:47]
	v_accvgpr_read_b32 v9, a36
	s_waitcnt lgkmcnt(1)
	v_mfma_f32_16x16x32_bf16 a[44:47], v[4:7], v[10:13], a[44:47]
	ds_read_b128 v[4:7], v44 offset:24576
	v_mfma_f32_16x16x32_bf16 a[44:47], v[30:33], v[26:29], a[44:47]
	ds_read_b128 v[30:33], v44 offset:25600
	s_waitcnt lgkmcnt(1)
	v_mfma_f32_16x16x32_bf16 a[48:51], v[4:7], v[18:21], a[48:51]
	ds_read_b128 v[4:7], v44 offset:26624
	s_waitcnt lgkmcnt(1)
	v_mfma_f32_16x16x32_bf16 a[48:51], v[30:33], v[22:25], a[48:51]
	s_waitcnt lgkmcnt(0)
	v_mfma_f32_16x16x32_bf16 a[48:51], v[4:7], v[10:13], a[48:51]
	ds_read_b128 v[4:7], v44 offset:28672
	v_mfma_f32_16x16x32_bf16 a[48:51], v[14:17], v[26:29], a[48:51]
	ds_read_b128 v[14:17], v44 offset:29696
	s_waitcnt lgkmcnt(1)
	v_mfma_f32_16x16x32_bf16 a[52:55], v[4:7], v[18:21], a[52:55]
	ds_read_b128 v[4:7], v44 offset:31744
	s_nop 3
	v_accvgpr_read_b32 v20, a49
	s_waitcnt lgkmcnt(1)
	v_mfma_f32_16x16x32_bf16 a[52:55], v[14:17], v[22:25], a[52:55]
	v_accvgpr_read_b32 v16, a46
	v_accvgpr_read_b32 v21, a48
	v_cvt_pk_bf16_f32 v20, v21, v20
	v_mfma_f32_16x16x32_bf16 a[52:55], v[0:3], v[10:13], a[52:55]
	v_accvgpr_read_b32 v0, a17
	v_accvgpr_read_b32 v1, a16
	v_cvt_pk_bf16_f32 v0, v1, v0
	v_accvgpr_read_b32 v1, a19
	v_accvgpr_read_b32 v2, a18
	v_mfma_f32_16x16x32_bf16 a[28:31], v[50:53], v[26:29], a[28:31]
	v_cvt_pk_bf16_f32 v1, v2, v1
	v_accvgpr_read_b32 v2, a21
	v_accvgpr_read_b32 v3, a20
	s_waitcnt lgkmcnt(0)
	v_mfma_f32_16x16x32_bf16 a[52:55], v[4:7], v[26:29], a[52:55]
	v_cvt_pk_bf16_f32 v2, v3, v2
	v_accvgpr_read_b32 v3, a23
	v_accvgpr_read_b32 v4, a22
	v_cvt_pk_bf16_f32 v3, v4, v3
	v_accvgpr_read_b32 v4, a25
	v_accvgpr_read_b32 v5, a24
	v_cvt_pk_bf16_f32 v4, v5, v4
	v_accvgpr_read_b32 v5, a27
	v_accvgpr_read_b32 v6, a26
	v_cvt_pk_bf16_f32 v5, v6, v5
	v_accvgpr_read_b32 v6, a29
	v_accvgpr_read_b32 v7, a28
	v_cvt_pk_bf16_f32 v6, v7, v6
	v_accvgpr_read_b32 v7, a31
	v_accvgpr_read_b32 v8, a30
	v_cvt_pk_bf16_f32 v7, v8, v7
	v_accvgpr_read_b32 v8, a37
	ds_read_b128 v[12:15], v44 offset:32768
	v_cvt_pk_bf16_f32 v8, v9, v8
	v_accvgpr_read_b32 v9, a39
	v_accvgpr_read_b32 v10, a38
	v_cvt_pk_bf16_f32 v9, v10, v9
	v_accvgpr_read_b32 v10, a45
	v_accvgpr_read_b32 v11, a44
	v_cvt_pk_bf16_f32 v10, v11, v10
	v_accvgpr_read_b32 v11, a47
	v_cvt_pk_bf16_f32 v11, v16, v11
	ds_read_b128 v[16:19], v44 offset:33792
	ds_read_b128 v[24:27], v44 offset:34816
	s_waitcnt lgkmcnt(2)
	v_mfma_f32_16x16x32_bf16 a[0:3], v[12:15], v[0:3], a[0:3]
	v_accvgpr_read_b32 v21, a51
	v_accvgpr_read_b32 v12, a50
	v_cvt_pk_bf16_f32 v21, v12, v21
	ds_read_b128 v[12:15], v44 offset:35840
	s_waitcnt lgkmcnt(2)
	v_mfma_f32_16x16x32_bf16 a[0:3], v[16:19], v[4:7], a[0:3]
	v_accvgpr_read_b32 v16, a53
	v_accvgpr_read_b32 v17, a52
	v_cvt_pk_bf16_f32 v22, v17, v16
	s_waitcnt lgkmcnt(1)
	v_mfma_f32_16x16x32_bf16 a[0:3], v[24:27], v[8:11], a[0:3]
	v_accvgpr_read_b32 v16, a55
	v_accvgpr_read_b32 v17, a54
	v_accvgpr_write_b32 a16, v164
	v_accvgpr_write_b32 a17, v165
	v_accvgpr_write_b32 a18, v166
	v_accvgpr_write_b32 a19, v167
	v_cvt_pk_bf16_f32 v23, v17, v16
	v_accvgpr_write_b32 a20, v180
	v_accvgpr_write_b32 a21, v181
	v_accvgpr_write_b32 a22, v182
	v_accvgpr_write_b32 a23, v183
	s_waitcnt lgkmcnt(0)
	v_mfma_f32_16x16x32_bf16 a[0:3], v[12:15], v[20:23], a[0:3]
	s_nop 7
	v_accvgpr_read_b32 v12, a0
	v_mul_f32_e32 v12, 0x4038aa3b, v12
	v_exp_f32_e32 v16, v12
	v_accvgpr_read_b32 v12, a1
	v_mul_f32_e32 v12, 0x4038aa3b, v12
	v_exp_f32_e32 v17, v12
	ds_read_b128 v[12:15], v44 offset:36864
	v_add_f32_e32 v16, 1.0, v16
	v_rcp_f32_e32 v28, v16
	v_add_f32_e32 v24, 1.0, v17
	ds_read_b128 v[16:19], v44 offset:37888
	v_rcp_f32_e32 v29, v24
	ds_read_b128 v[24:27], v44 offset:38912
	s_waitcnt lgkmcnt(2)
	v_mfma_f32_16x16x32_bf16 a[24:27], v[12:15], v[0:3], a[56:59]
	v_accvgpr_read_b32 v30, a2
	v_mul_f32_e32 v12, 0x4038aa3b, v30
	v_exp_f32_e32 v30, v12
	ds_read_b128 v[12:15], v44 offset:39936
	s_waitcnt lgkmcnt(2)
	v_mfma_f32_16x16x32_bf16 a[24:27], v[16:19], v[4:7], a[24:27]
	v_accvgpr_read_b32 v16, a3
	v_mul_f32_e32 v16, 0x4038aa3b, v16
	v_exp_f32_e32 v17, v16
	s_waitcnt lgkmcnt(1)
	v_mfma_f32_16x16x32_bf16 a[0:3], v[24:27], v[8:11], a[24:27]
	v_add_f32_e32 v16, 1.0, v30
	v_rcp_f32_e32 v16, v16
	v_add_f32_e32 v17, 1.0, v17
	s_waitcnt lgkmcnt(0)
	v_mfma_f32_16x16x32_bf16 a[0:3], v[12:15], v[20:23], a[0:3]
	v_rcp_f32_e32 v17, v17
	v_pk_fma_f32 v[28:29], v[28:29], -2.0, 1.0 op_sel_hi:[1,0,0]
	v_pk_fma_f32 v[30:31], v[16:17], -2.0, 1.0 op_sel_hi:[1,0,0]
	s_nop 4
	v_accvgpr_read_b32 v12, a0
	v_mul_f32_e32 v12, 0x4038aa3b, v12
	v_accvgpr_read_b32 v13, a1
	v_exp_f32_e32 v12, v12
	v_mul_f32_e32 v13, 0x4038aa3b, v13
	v_exp_f32_e32 v13, v13
	v_accvgpr_read_b32 v35, a3
	v_add_f32_e32 v12, 1.0, v12
	v_rcp_f32_e32 v24, v12
	v_add_f32_e32 v18, 1.0, v13
	ds_read_b128 v[12:15], v44 offset:40960
	v_rcp_f32_e32 v25, v18
	ds_read_b128 v[16:19], v44 offset:41984
	s_waitcnt lgkmcnt(1)
	v_mfma_f32_16x16x32_bf16 a[4:7], v[12:15], v[0:3], a[4:7]
	v_fma_f32 v32, v24, -2.0, 1.0
	v_fma_f32 v33, v25, -2.0, 1.0
	v_accvgpr_read_b32 v24, a2
	v_mul_f32_e32 v34, 0x4038aa3b, v24
	ds_read_b128 v[24:27], v44 offset:43008
	ds_read_b128 v[12:15], v44 offset:44032
	s_waitcnt lgkmcnt(2)
	v_mfma_f32_16x16x32_bf16 a[0:3], v[16:19], v[4:7], a[4:7]
	v_mul_f32_e32 v16, 0x4038aa3b, v35
	v_exp_f32_e32 v16, v16
	v_exp_f32_e32 v34, v34
	s_waitcnt lgkmcnt(1)
	v_mfma_f32_16x16x32_bf16 a[0:3], v[24:27], v[8:11], a[0:3]
	v_add_f32_e32 v16, 1.0, v16
	v_rcp_f32_e32 v35, v16
	v_add_f32_e32 v17, 1.0, v34
	s_waitcnt lgkmcnt(0)
	v_mfma_f32_16x16x32_bf16 a[0:3], v[12:15], v[20:23], a[0:3]
	v_rcp_f32_e32 v34, v17
	v_accvgpr_write_b32 a4, v188
	v_accvgpr_write_b32 a5, v189
	v_accvgpr_write_b32 a6, v190
	v_accvgpr_write_b32 a7, v191
	v_pk_fma_f32 v[34:35], v[34:35], -2.0, 1.0 op_sel_hi:[1,0,0]
	s_nop 4
	v_accvgpr_read_b32 v12, a0
	v_mul_f32_e32 v12, 0x4038aa3b, v12
	v_exp_f32_e32 v16, v12
	v_accvgpr_read_b32 v12, a1
	v_mul_f32_e32 v12, 0x4038aa3b, v12
	v_exp_f32_e32 v17, v12
	ds_read_b128 v[12:15], v44 offset:45056
	v_add_f32_e32 v16, 1.0, v16
	v_rcp_f32_e32 v36, v16
	v_add_f32_e32 v24, 1.0, v17
	ds_read_b128 v[16:19], v44 offset:46080
	v_rcp_f32_e32 v37, v24
	ds_read_b128 v[24:27], v44 offset:47104
	s_waitcnt lgkmcnt(2)
	v_mfma_f32_16x16x32_bf16 a[16:19], v[12:15], v[0:3], a[16:19]
	v_accvgpr_read_b32 v38, a2
	v_mul_f32_e32 v12, 0x4038aa3b, v38
	v_exp_f32_e32 v38, v12
	ds_read_b128 v[12:15], v44 offset:48128
	s_waitcnt lgkmcnt(2)
	v_mfma_f32_16x16x32_bf16 a[16:19], v[16:19], v[4:7], a[16:19]
	v_accvgpr_read_b32 v17, a3
	v_mul_f32_e32 v17, 0x4038aa3b, v17
	v_exp_f32_e32 v17, v17
	s_waitcnt lgkmcnt(1)
	v_mfma_f32_16x16x32_bf16 a[16:19], v[24:27], v[8:11], a[16:19]
	v_add_f32_e32 v16, 1.0, v38
	v_rcp_f32_e32 v38, v16
	v_pk_fma_f32 v[36:37], v[36:37], -2.0, 1.0 op_sel_hi:[1,0,0]
	s_waitcnt lgkmcnt(0)
	v_mfma_f32_16x16x32_bf16 a[0:3], v[12:15], v[20:23], a[16:19]
	v_add_f32_e32 v13, 1.0, v17
	v_rcp_f32_e32 v39, v13
	s_nop 0
	v_pk_fma_f32 v[38:39], v[38:39], -2.0, 1.0 op_sel_hi:[1,0,0]
	s_nop 3
	v_accvgpr_read_b32 v12, a0
	v_mul_f32_e32 v12, 0x4038aa3b, v12
	v_exp_f32_e32 v12, v12
	v_accvgpr_read_b32 v17, a2
	v_mul_f32_e32 v17, 0x4038aa3b, v17
	v_exp_f32_e32 v24, v17
	v_add_f32_e32 v12, 1.0, v12
	v_rcp_f32_e32 v40, v12
	v_accvgpr_read_b32 v12, a1
	v_mul_f32_e32 v12, 0x4038aa3b, v12
	v_exp_f32_e32 v16, v12
	ds_read_b128 v[12:15], v44 offset:49152
	v_add_f32_e32 v42, 1.0, v24
	v_accvgpr_read_b32 v43, a3
	v_add_f32_e32 v25, 1.0, v16
	ds_read_b128 v[16:19], v44 offset:50176
	v_rcp_f32_e32 v41, v25
	ds_read_b128 v[24:27], v44 offset:51200
	s_waitcnt lgkmcnt(2)
	v_mfma_f32_16x16x32_bf16 a[0:3], v[12:15], v[0:3], a[32:35]
	v_mul_f32_e32 v12, 0x4038aa3b, v43
	v_exp_f32_e32 v43, v12
	ds_read_b128 v[12:15], v44 offset:52224
	s_waitcnt lgkmcnt(2)
	v_mfma_f32_16x16x32_bf16 a[0:3], v[16:19], v[4:7], a[0:3]
	v_rcp_f32_e32 v16, v42
	v_add_f32_e32 v17, 1.0, v43
	v_rcp_f32_e32 v17, v17
	s_waitcnt lgkmcnt(1)
	v_mfma_f32_16x16x32_bf16 a[0:3], v[24:27], v[8:11], a[0:3]
	v_fma_f32 v40, v40, -2.0, 1.0
	v_fma_f32 v41, v41, -2.0, 1.0
	v_pk_fma_f32 v[42:43], v[16:17], -2.0, 1.0 op_sel_hi:[1,0,0]
	s_waitcnt lgkmcnt(0)
	v_mfma_f32_16x16x32_bf16 a[0:3], v[12:15], v[20:23], a[0:3]
	s_nop 7
	v_accvgpr_read_b32 v12, a0
	v_mul_f32_e32 v12, 0x4038aa3b, v12
	v_exp_f32_e32 v16, v12
	v_accvgpr_read_b32 v12, a1
	v_mul_f32_e32 v17, 0x4038aa3b, v12
	ds_read_b128 v[12:15], v44 offset:53248
	v_exp_f32_e32 v24, v17
	v_add_f32_e32 v16, 1.0, v16
	v_rcp_f32_e32 v50, v16
	ds_read_b128 v[16:19], v44 offset:54272
	v_add_f32_e32 v24, 1.0, v24
	v_rcp_f32_e32 v51, v24
	ds_read_b128 v[24:27], v44 offset:55296
	s_waitcnt lgkmcnt(2)
	v_mfma_f32_16x16x32_bf16 a[16:19], v[12:15], v[0:3], a[40:43]
	v_accvgpr_read_b32 v52, a2
	v_mul_f32_e32 v0, 0x4038aa3b, v52
	v_exp_f32_e32 v12, v0
	ds_read_b128 v[0:3], v44 offset:56320
	s_waitcnt lgkmcnt(2)
	v_mfma_f32_16x16x32_bf16 a[16:19], v[16:19], v[4:7], a[16:19]
	v_accvgpr_read_b32 v4, a3
	v_mul_f32_e32 v4, 0x4038aa3b, v4
	v_exp_f32_e32 v5, v4
	s_waitcnt lgkmcnt(1)
	v_mfma_f32_16x16x32_bf16 a[0:3], v[24:27], v[8:11], a[16:19]
	v_add_f32_e32 v4, 1.0, v12
	ds_read_b128 v[10:13], v44 offset:57344
	v_add_f32_e32 v5, 1.0, v5
	s_waitcnt lgkmcnt(1)
	v_mfma_f32_16x16x32_bf16 a[0:3], v[0:3], v[20:23], a[0:3]
	v_rcp_f32_e32 v4, v4
	v_rcp_f32_e32 v5, v5
	ds_read_b128 v[18:21], v44 offset:58368
	v_pk_fma_f32 v[14:15], v[50:51], -2.0, 1.0 op_sel_hi:[1,0,0]
	v_cvt_pk_bf16_f32 v6, v36, v37
	v_pk_fma_f32 v[16:17], v[4:5], -2.0, 1.0 op_sel_hi:[1,0,0]
	v_cvt_pk_bf16_f32 v4, v32, v33
	v_cvt_pk_bf16_f32 v5, v34, v35
	v_accvgpr_read_b32 v2, a2
	v_accvgpr_read_b32 v3, a3
	v_mul_f32_e32 v2, 0x4038aa3b, v2
	v_mul_f32_e32 v3, 0x4038aa3b, v3
	v_exp_f32_e32 v2, v2
	v_exp_f32_e32 v3, v3
	v_accvgpr_read_b32 v0, a0
	v_accvgpr_read_b32 v1, a1
	v_add_f32_e32 v2, 1.0, v2
	v_add_f32_e32 v3, 1.0, v3
	v_rcp_f32_e32 v2, v2
	v_rcp_f32_e32 v3, v3
	v_mul_f32_e32 v0, 0x4038aa3b, v0
	v_mul_f32_e32 v1, 0x4038aa3b, v1
	v_exp_f32_e32 v0, v0
	v_exp_f32_e32 v1, v1
	v_pk_fma_f32 v[22:23], v[2:3], -2.0, 1.0 op_sel_hi:[1,0,0]
	v_cvt_pk_bf16_f32 v2, v28, v29
	v_cvt_pk_bf16_f32 v3, v30, v31
	v_cvt_pk_bf16_f32 v14, v14, v15
	v_cvt_pk_bf16_f32 v15, v16, v17
	v_cvt_pk_bf16_f32 v17, v22, v23
	ds_read_b128 v[22:25], v44 offset:59392
	s_waitcnt lgkmcnt(2)
	v_mfma_f32_16x16x32_bf16 a[0:3], v[10:13], v[2:5], a[8:11]
	ds_read_b128 v[10:13], v44 offset:60416
	v_add_f32_e32 v0, 1.0, v0
	v_add_f32_e32 v1, 1.0, v1
	v_rcp_f32_e32 v0, v0
	v_rcp_f32_e32 v1, v1
	v_cvt_pk_bf16_f32 v7, v38, v39
	v_cvt_pk_bf16_f32 v8, v40, v41
	v_cvt_pk_bf16_f32 v9, v42, v43
	v_pk_fma_f32 v[0:1], v[0:1], -2.0, 1.0 op_sel_hi:[1,0,0]
	s_waitcnt lgkmcnt(0)
	v_mfma_f32_16x16x32_bf16 a[8:11], v[10:13], v[2:5], a[20:23]
	v_cvt_pk_bf16_f32 v16, v0, v1
	v_mov_b32_e32 v0, 0x11000
	v_mad_u32_u24 v0, v56, s0, v0
	v_mfma_f32_16x16x32_bf16 a[0:3], v[18:21], v[6:9], a[0:3]
	ds_read_b128 v[18:21], v44 offset:61440
	v_mad_u32_u24 v1, v57, s2, v0
	v_add_u32_e32 v26, v1, v48
	v_mfma_f32_16x16x32_bf16 a[0:3], v[22:25], v[14:17], a[0:3]
	ds_read_b128 v[22:25], v44 offset:62464
	s_waitcnt lgkmcnt(1)
	v_mfma_f32_16x16x32_bf16 a[8:11], v[18:21], v[6:9], a[8:11]
	ds_read_b128 v[18:21], v44 offset:64512
	s_nop 3
	v_accvgpr_read_b32 v27, a1
	v_accvgpr_read_b32 v10, a0
	ds_write2_b32 v26, v10, v27 offset0:1 offset1:2
	v_accvgpr_read_b32 v10, a3
	v_accvgpr_read_b32 v11, a2
	ds_write2_b32 v26, v11, v10 offset0:3 offset1:4
	ds_read_b128 v[10:13], v44 offset:63488
	s_waitcnt lgkmcnt(4)
	v_mfma_f32_16x16x32_bf16 a[0:3], v[22:25], v[14:17], a[8:11]
	s_nop 7
	v_accvgpr_read_b32 v22, a1
	v_accvgpr_read_b32 v23, a0
	ds_write2_b32 v26, v23, v22 offset0:17 offset1:18
	v_or_b32_e32 v22, 0x10000, v44
	ds_read_b128 v[22:25], v22
	s_waitcnt lgkmcnt(2)
	v_mfma_f32_16x16x32_bf16 a[8:11], v[10:13], v[2:5], a[12:15]
	v_or_b32_e32 v10, 0x10400, v44
	ds_read_b128 v[10:13], v10
	v_accvgpr_read_b32 v27, a3
	v_mfma_f32_16x16x32_bf16 a[8:11], v[18:21], v[6:9], a[8:11]
	v_or_b32_e32 v18, 0x10800, v44
	ds_read_b128 v[18:21], v18
	v_accvgpr_read_b32 v28, a2
	s_waitcnt lgkmcnt(2)
	v_mfma_f32_16x16x32_bf16 a[0:3], v[22:25], v[14:17], a[8:11]
	v_or_b32_e32 v22, 0x10c00, v44
	ds_read_b128 v[22:25], v22
	ds_write2_b32 v26, v28, v27 offset0:19 offset1:20
	s_waitcnt lgkmcnt(3)
	v_mfma_f32_16x16x32_bf16 a[4:7], v[10:13], v[2:5], a[4:7]
	s_waitcnt lgkmcnt(2)
	v_mfma_f32_16x16x32_bf16 a[4:7], v[18:21], v[6:9], a[4:7]
	s_nop 0
	v_accvgpr_read_b32 v2, a1
	v_accvgpr_read_b32 v3, a0
	ds_write2_b32 v26, v3, v2 offset0:33 offset1:34
	v_accvgpr_read_b32 v2, a3
	v_accvgpr_read_b32 v3, a2
	s_waitcnt lgkmcnt(2)
	v_mfma_f32_16x16x32_bf16 a[0:3], v[22:25], v[14:17], a[4:7]
	ds_write2_b32 v26, v3, v2 offset0:35 offset1:36
	s_nop 6
	v_accvgpr_read_b32 v2, a1
	v_accvgpr_read_b32 v3, a0
	ds_write2_b32 v26, v3, v2 offset0:49 offset1:50
	v_accvgpr_read_b32 v2, a3
	v_accvgpr_read_b32 v3, a2
	ds_write2_b32 v26, v3, v2 offset0:51 offset1:52
	s_and_saveexec_b64 s[0:1], vcc
	ds_write_b32 v1, v46
	s_or_b64 exec, exec, s[0:1]
	v_add_u32_e32 v2, v0, v44
	v_mov_b64_e32 v[0:1], s[10:11]
	v_mad_u64_u32 v[0:1], s[0:1], v47, s2, v[0:1]
	ds_read_b128 v[4:7], v2
	v_lshl_add_u64 v[8:9], v[0:1], 0, v[44:45]
	s_waitcnt lgkmcnt(0)
	global_store_dwordx4 v[8:9], v[4:7], off sc1
	s_nop 1
	s_mov_b64 s[0:1], 0x400
	ds_read_b128 v[4:7], v2 offset:1024
	v_lshl_add_u64 v[10:11], v[8:9], 0, s[0:1]
	s_waitcnt lgkmcnt(0)
	global_store_dwordx4 v[10:11], v[4:7], off sc1
	s_nop 1
	s_mov_b64 s[0:1], 0x800
	ds_read_b128 v[4:7], v2 offset:2048
	v_lshl_add_u64 v[10:11], v[8:9], 0, s[0:1]
	s_waitcnt lgkmcnt(0)
	global_store_dwordx4 v[10:11], v[4:7], off sc1
	s_nop 1
	s_mov_b64 s[0:1], 0xc00
	ds_read_b128 v[4:7], v2 offset:3072
	v_lshl_add_u64 v[8:9], v[8:9], 0, s[0:1]
	s_waitcnt lgkmcnt(0)
	global_store_dwordx4 v[8:9], v[4:7], off sc1
	s_nop 1
	v_or_b32_e32 v3, 0x100, v49
	v_cmp_gt_u32_e32 vcc, s2, v3
	s_and_saveexec_b64 s[0:1], vcc
	s_cbranch_execz .LBB2_4
	ds_read_b128 v[4:7], v2 offset:4096
	v_lshlrev_b32_e32 v2, 4, v3
	v_mov_b32_e32 v3, 0
	v_lshl_add_u64 v[0:1], v[0:1], 0, v[2:3]
	s_waitcnt lgkmcnt(0)
	global_store_dwordx4 v[0:1], v[4:7], off sc1
	s_nop 1
